# LSTM layer-1 launch, spare blocks: skip-feature FC path rewritten (both tiles of a wave processed together, weight fragments loaded once, loads pipelined 2-4 timesteps ahead instead of a wait per load
# speedup vs baseline: 1.0025x; 1.0020x over previous
.LBB6_33:
	s_and_b64 vcc, exec, s[4:5]
	s_cbranch_vccz .LBB6_39
	s_load_dwordx4 s[4:7], s[0:1], 0x30
	s_load_dwordx2 s[8:9], s[0:1], 0x60
	s_lshl_b32 s3, s2, 3
	s_addk_i32 s3, 0xf978
	v_or_b32_e32 v1, s3, v195
	v_and_b32_e32 v2, 15, v0
	v_bfe_u32 v3, v0, 4, 2
	v_readfirstlane_b32 s20, v1
	v_and_b32_e32 v1, 63, v0
	v_lshlrev_b32_e32 v166, 4, v1
	v_add_u32_e32 v167, 0x1000, v166
	s_nop 1
	s_add_i32 s21, s20, 0x178
	s_cmpk_lt_i32 s21, 0x271
	s_cselect_b32 s22, s21, s20
	s_cselect_b32 s23, 1, 0
	s_lshl_b32 s20, s20, 4
	s_lshl_b32 s22, s22, 4
	v_add_u32_e32 v1, s20, v2
	v_add_u32_e32 v2, s22, v2
	v_lshlrev_b32_e32 v164, 6, v1
	v_lshlrev_b32_e32 v165, 6, v2
	v_lshl_add_u32 v164, v3, 4, v164
	v_lshl_add_u32 v165, v3, 4, v165
	v_lshlrev_b32_e32 v168, 9, v1
	v_lshlrev_b32_e32 v169, 9, v2
	v_lshl_add_u32 v168, v3, 4, v168
	v_lshl_add_u32 v169, v3, 4, v169
	v_mov_b32_e32 v4, 0
	v_mov_b32_e32 v5, 0
	v_mov_b32_e32 v6, 0
	v_mov_b32_e32 v7, 0
	v_mov_b32_e32 v8, 0
	v_mov_b32_e32 v9, 0
	v_mov_b32_e32 v10, 0
	v_mov_b32_e32 v11, 0
	v_mov_b32_e32 v12, 0
	v_mov_b32_e32 v13, 0
	v_mov_b32_e32 v14, 0
	v_mov_b32_e32 v15, 0
	v_mov_b32_e32 v16, 0
	v_mov_b32_e32 v17, 0
	v_mov_b32_e32 v18, 0
	v_mov_b32_e32 v19, 0
	v_mov_b32_e32 v20, 0
	v_mov_b32_e32 v21, 0
	v_mov_b32_e32 v22, 0
	v_mov_b32_e32 v23, 0
	v_mov_b32_e32 v24, 0
	v_mov_b32_e32 v25, 0
	v_mov_b32_e32 v26, 0
	v_mov_b32_e32 v27, 0
	v_mov_b32_e32 v28, 0
	v_mov_b32_e32 v29, 0
	v_mov_b32_e32 v30, 0
	v_mov_b32_e32 v31, 0
	v_mov_b32_e32 v32, 0
	v_mov_b32_e32 v33, 0
	v_mov_b32_e32 v34, 0
	v_mov_b32_e32 v35, 0
	v_mov_b32_e32 v36, 0
	v_mov_b32_e32 v37, 0
	v_mov_b32_e32 v38, 0
	v_mov_b32_e32 v39, 0
	v_mov_b32_e32 v40, 0
	v_mov_b32_e32 v41, 0
	v_mov_b32_e32 v42, 0
	v_mov_b32_e32 v43, 0
	v_mov_b32_e32 v44, 0
	v_mov_b32_e32 v45, 0
	v_mov_b32_e32 v46, 0
	v_mov_b32_e32 v47, 0
	v_mov_b32_e32 v48, 0
	v_mov_b32_e32 v49, 0
	v_mov_b32_e32 v50, 0
	v_mov_b32_e32 v51, 0
	v_mov_b32_e32 v52, 0
	v_mov_b32_e32 v53, 0
	v_mov_b32_e32 v54, 0
	v_mov_b32_e32 v55, 0
	v_mov_b32_e32 v56, 0
	v_mov_b32_e32 v57, 0
	v_mov_b32_e32 v58, 0
	v_mov_b32_e32 v59, 0
	v_mov_b32_e32 v60, 0
	v_mov_b32_e32 v61, 0
	v_mov_b32_e32 v62, 0
	v_mov_b32_e32 v63, 0
	v_mov_b32_e32 v64, 0
	v_mov_b32_e32 v65, 0
	v_mov_b32_e32 v66, 0
	v_mov_b32_e32 v67, 0
	s_waitcnt lgkmcnt(0)
	s_add_u32 s6, s6, 0x10000
	s_addc_u32 s7, s7, 0
	s_mov_b32 s10, s4
	s_mov_b32 s11, s5
	global_load_dwordx4 v[68:71], v164, s[10:11]
	global_load_dwordx4 v[84:87], v165, s[10:11]
	s_add_u32 s10, s10, 0x9c400
	s_addc_u32 s11, s11, 0
	global_load_dwordx4 v[72:75], v164, s[10:11]
	global_load_dwordx4 v[88:91], v165, s[10:11]
	s_add_u32 s10, s10, 0x9c400
	s_addc_u32 s11, s11, 0
	global_load_dwordx4 v[76:79], v164, s[10:11]
	global_load_dwordx4 v[92:95], v165, s[10:11]
	s_add_u32 s10, s10, 0x9c400
	s_addc_u32 s11, s11, 0
	global_load_dwordx4 v[80:83], v164, s[10:11]
	global_load_dwordx4 v[96:99], v165, s[10:11]
	s_add_u32 s10, s10, 0x9c400
	s_addc_u32 s11, s11, 0
	global_load_dwordx4 v[100:103], v166, s[6:7] offset:0
	global_load_dwordx4 v[104:107], v166, s[6:7] offset:1024
	global_load_dwordx4 v[108:111], v166, s[6:7] offset:2048
	global_load_dwordx4 v[112:115], v166, s[6:7] offset:3072
	global_load_dwordx4 v[116:119], v167, s[6:7] offset:0
	global_load_dwordx4 v[120:123], v167, s[6:7] offset:1024
	global_load_dwordx4 v[124:127], v167, s[6:7] offset:2048
	global_load_dwordx4 v[128:131], v167, s[6:7] offset:3072
	s_add_u32 s6, s6, 0x2000
	s_addc_u32 s7, s7, 0
	global_load_dwordx4 v[132:135], v166, s[6:7] offset:0
	global_load_dwordx4 v[136:139], v166, s[6:7] offset:1024
	global_load_dwordx4 v[140:143], v166, s[6:7] offset:2048
	global_load_dwordx4 v[144:147], v166, s[6:7] offset:3072
	global_load_dwordx4 v[148:151], v167, s[6:7] offset:0
	global_load_dwordx4 v[152:155], v167, s[6:7] offset:1024
	global_load_dwordx4 v[156:159], v167, s[6:7] offset:2048
	global_load_dwordx4 v[160:163], v167, s[6:7] offset:3072
	s_add_u32 s6, s6, 0x2000
	s_addc_u32 s7, s7, 0
	s_waitcnt vmcnt(22)
	s_waitcnt vmcnt(15)
	v_mfma_f32_16x16x32_f16 v[4:7], v[100:103], v[68:71], v[4:7]
	v_mfma_f32_16x16x32_f16 v[36:39], v[100:103], v[84:87], v[36:39]
	s_waitcnt vmcnt(14)
	v_mfma_f32_16x16x32_f16 v[8:11], v[104:107], v[68:71], v[8:11]
	v_mfma_f32_16x16x32_f16 v[40:43], v[104:107], v[84:87], v[40:43]
	s_waitcnt vmcnt(13)
	v_mfma_f32_16x16x32_f16 v[12:15], v[108:111], v[68:71], v[12:15]
	v_mfma_f32_16x16x32_f16 v[44:47], v[108:111], v[84:87], v[44:47]
	s_waitcnt vmcnt(12)
	v_mfma_f32_16x16x32_f16 v[16:19], v[112:115], v[68:71], v[16:19]
	v_mfma_f32_16x16x32_f16 v[48:51], v[112:115], v[84:87], v[48:51]
	s_waitcnt vmcnt(11)
	v_mfma_f32_16x16x32_f16 v[20:23], v[116:119], v[68:71], v[20:23]
	v_mfma_f32_16x16x32_f16 v[52:55], v[116:119], v[84:87], v[52:55]
	s_waitcnt vmcnt(10)
	v_mfma_f32_16x16x32_f16 v[24:27], v[120:123], v[68:71], v[24:27]
	v_mfma_f32_16x16x32_f16 v[56:59], v[120:123], v[84:87], v[56:59]
	s_waitcnt vmcnt(9)
	v_mfma_f32_16x16x32_f16 v[28:31], v[124:127], v[68:71], v[28:31]
	v_mfma_f32_16x16x32_f16 v[60:63], v[124:127], v[84:87], v[60:63]
	s_waitcnt vmcnt(8)
	v_mfma_f32_16x16x32_f16 v[32:35], v[128:131], v[68:71], v[32:35]
	v_mfma_f32_16x16x32_f16 v[64:67], v[128:131], v[84:87], v[64:67]
	global_load_dwordx4 v[100:103], v166, s[6:7] offset:0
	global_load_dwordx4 v[104:107], v166, s[6:7] offset:1024
	global_load_dwordx4 v[108:111], v166, s[6:7] offset:2048
	global_load_dwordx4 v[112:115], v166, s[6:7] offset:3072
	global_load_dwordx4 v[116:119], v167, s[6:7] offset:0
	global_load_dwordx4 v[120:123], v167, s[6:7] offset:1024
	global_load_dwordx4 v[124:127], v167, s[6:7] offset:2048
	global_load_dwordx4 v[128:131], v167, s[6:7] offset:3072
	s_add_u32 s6, s6, 0x2000
	s_addc_u32 s7, s7, 0
	global_load_dwordx4 v[68:71], v164, s[10:11]
	global_load_dwordx4 v[84:87], v165, s[10:11]
	s_add_u32 s10, s10, 0x9c400
	s_addc_u32 s11, s11, 0
	s_waitcnt vmcnt(17)
	v_mfma_f32_16x16x32_f16 v[4:7], v[132:135], v[72:75], v[4:7]
	v_mfma_f32_16x16x32_f16 v[36:39], v[132:135], v[88:91], v[36:39]
	s_waitcnt vmcnt(16)
	v_mfma_f32_16x16x32_f16 v[8:11], v[136:139], v[72:75], v[8:11]
	v_mfma_f32_16x16x32_f16 v[40:43], v[136:139], v[88:91], v[40:43]
	s_waitcnt vmcnt(15)
	v_mfma_f32_16x16x32_f16 v[12:15], v[140:143], v[72:75], v[12:15]
	v_mfma_f32_16x16x32_f16 v[44:47], v[140:143], v[88:91], v[44:47]
	s_waitcnt vmcnt(14)
	v_mfma_f32_16x16x32_f16 v[16:19], v[144:147], v[72:75], v[16:19]
	v_mfma_f32_16x16x32_f16 v[48:51], v[144:147], v[88:91], v[48:51]
	s_waitcnt vmcnt(13)
	v_mfma_f32_16x16x32_f16 v[20:23], v[148:151], v[72:75], v[20:23]
	v_mfma_f32_16x16x32_f16 v[52:55], v[148:151], v[88:91], v[52:55]
	s_waitcnt vmcnt(12)
	v_mfma_f32_16x16x32_f16 v[24:27], v[152:155], v[72:75], v[24:27]
	v_mfma_f32_16x16x32_f16 v[56:59], v[152:155], v[88:91], v[56:59]
	s_waitcnt vmcnt(11)
	v_mfma_f32_16x16x32_f16 v[28:31], v[156:159], v[72:75], v[28:31]
	v_mfma_f32_16x16x32_f16 v[60:63], v[156:159], v[88:91], v[60:63]
	s_waitcnt vmcnt(10)
	v_mfma_f32_16x16x32_f16 v[32:35], v[160:163], v[72:75], v[32:35]
	v_mfma_f32_16x16x32_f16 v[64:67], v[160:163], v[88:91], v[64:67]
	global_load_dwordx4 v[132:135], v166, s[6:7] offset:0
	global_load_dwordx4 v[136:139], v166, s[6:7] offset:1024
	global_load_dwordx4 v[140:143], v166, s[6:7] offset:2048
	global_load_dwordx4 v[144:147], v166, s[6:7] offset:3072
	global_load_dwordx4 v[148:151], v167, s[6:7] offset:0
	global_load_dwordx4 v[152:155], v167, s[6:7] offset:1024
	global_load_dwordx4 v[156:159], v167, s[6:7] offset:2048
	global_load_dwordx4 v[160:163], v167, s[6:7] offset:3072
	s_add_u32 s6, s6, 0x2000
	s_addc_u32 s7, s7, 0
	global_load_dwordx4 v[72:75], v164, s[10:11]
	global_load_dwordx4 v[88:91], v165, s[10:11]
	s_add_u32 s10, s10, 0x9c400
	s_addc_u32 s11, s11, 0
	s_waitcnt vmcnt(19)
	v_mfma_f32_16x16x32_f16 v[4:7], v[100:103], v[76:79], v[4:7]
	v_mfma_f32_16x16x32_f16 v[36:39], v[100:103], v[92:95], v[36:39]
	s_waitcnt vmcnt(18)
	v_mfma_f32_16x16x32_f16 v[8:11], v[104:107], v[76:79], v[8:11]
	v_mfma_f32_16x16x32_f16 v[40:43], v[104:107], v[92:95], v[40:43]
	s_waitcnt vmcnt(17)
	v_mfma_f32_16x16x32_f16 v[12:15], v[108:111], v[76:79], v[12:15]
	v_mfma_f32_16x16x32_f16 v[44:47], v[108:111], v[92:95], v[44:47]
	s_waitcnt vmcnt(16)
	v_mfma_f32_16x16x32_f16 v[16:19], v[112:115], v[76:79], v[16:19]
	v_mfma_f32_16x16x32_f16 v[48:51], v[112:115], v[92:95], v[48:51]
	s_waitcnt vmcnt(15)
	v_mfma_f32_16x16x32_f16 v[20:23], v[116:119], v[76:79], v[20:23]
	v_mfma_f32_16x16x32_f16 v[52:55], v[116:119], v[92:95], v[52:55]
	s_waitcnt vmcnt(14)
	v_mfma_f32_16x16x32_f16 v[24:27], v[120:123], v[76:79], v[24:27]
	v_mfma_f32_16x16x32_f16 v[56:59], v[120:123], v[92:95], v[56:59]
	s_waitcnt vmcnt(13)
	v_mfma_f32_16x16x32_f16 v[28:31], v[124:127], v[76:79], v[28:31]
	v_mfma_f32_16x16x32_f16 v[60:63], v[124:127], v[92:95], v[60:63]
	s_waitcnt vmcnt(12)
	v_mfma_f32_16x16x32_f16 v[32:35], v[128:131], v[76:79], v[32:35]
	v_mfma_f32_16x16x32_f16 v[64:67], v[128:131], v[92:95], v[64:67]
	global_load_dwordx4 v[100:103], v166, s[6:7] offset:0
	global_load_dwordx4 v[104:107], v166, s[6:7] offset:1024
	global_load_dwordx4 v[108:111], v166, s[6:7] offset:2048
	global_load_dwordx4 v[112:115], v166, s[6:7] offset:3072
	global_load_dwordx4 v[116:119], v167, s[6:7] offset:0
	global_load_dwordx4 v[120:123], v167, s[6:7] offset:1024
	global_load_dwordx4 v[124:127], v167, s[6:7] offset:2048
	global_load_dwordx4 v[128:131], v167, s[6:7] offset:3072
	s_add_u32 s6, s6, 0x2000
	s_addc_u32 s7, s7, 0
	global_load_dwordx4 v[76:79], v164, s[10:11]
	global_load_dwordx4 v[92:95], v165, s[10:11]
	s_add_u32 s10, s10, 0x9c400
	s_addc_u32 s11, s11, 0
	s_waitcnt vmcnt(19)
	v_mfma_f32_16x16x32_f16 v[4:7], v[132:135], v[80:83], v[4:7]
	v_mfma_f32_16x16x32_f16 v[36:39], v[132:135], v[96:99], v[36:39]
	s_waitcnt vmcnt(18)
	v_mfma_f32_16x16x32_f16 v[8:11], v[136:139], v[80:83], v[8:11]
	v_mfma_f32_16x16x32_f16 v[40:43], v[136:139], v[96:99], v[40:43]
	s_waitcnt vmcnt(17)
	v_mfma_f32_16x16x32_f16 v[12:15], v[140:143], v[80:83], v[12:15]
	v_mfma_f32_16x16x32_f16 v[44:47], v[140:143], v[96:99], v[44:47]
	s_waitcnt vmcnt(16)
	v_mfma_f32_16x16x32_f16 v[16:19], v[144:147], v[80:83], v[16:19]
	v_mfma_f32_16x16x32_f16 v[48:51], v[144:147], v[96:99], v[48:51]
	s_waitcnt vmcnt(15)
	v_mfma_f32_16x16x32_f16 v[20:23], v[148:151], v[80:83], v[20:23]
	v_mfma_f32_16x16x32_f16 v[52:55], v[148:151], v[96:99], v[52:55]
	s_waitcnt vmcnt(14)
	v_mfma_f32_16x16x32_f16 v[24:27], v[152:155], v[80:83], v[24:27]
	v_mfma_f32_16x16x32_f16 v[56:59], v[152:155], v[96:99], v[56:59]
	s_waitcnt vmcnt(13)
	v_mfma_f32_16x16x32_f16 v[28:31], v[156:159], v[80:83], v[28:31]
	v_mfma_f32_16x16x32_f16 v[60:63], v[156:159], v[96:99], v[60:63]
	s_waitcnt vmcnt(12)
	v_mfma_f32_16x16x32_f16 v[32:35], v[160:163], v[80:83], v[32:35]
	v_mfma_f32_16x16x32_f16 v[64:67], v[160:163], v[96:99], v[64:67]
	global_load_dwordx4 v[132:135], v166, s[6:7] offset:0
	global_load_dwordx4 v[136:139], v166, s[6:7] offset:1024
	global_load_dwordx4 v[140:143], v166, s[6:7] offset:2048
	global_load_dwordx4 v[144:147], v166, s[6:7] offset:3072
	global_load_dwordx4 v[148:151], v167, s[6:7] offset:0
	global_load_dwordx4 v[152:155], v167, s[6:7] offset:1024
	global_load_dwordx4 v[156:159], v167, s[6:7] offset:2048
	global_load_dwordx4 v[160:163], v167, s[6:7] offset:3072
	s_add_u32 s6, s6, 0x2000
	s_addc_u32 s7, s7, 0
	global_load_dwordx4 v[80:83], v164, s[10:11]
	global_load_dwordx4 v[96:99], v165, s[10:11]
	s_add_u32 s10, s10, 0x9c400
	s_addc_u32 s11, s11, 0
	s_waitcnt vmcnt(19)
	v_mfma_f32_16x16x32_f16 v[4:7], v[100:103], v[68:71], v[4:7]
	v_mfma_f32_16x16x32_f16 v[36:39], v[100:103], v[84:87], v[36:39]
	s_waitcnt vmcnt(18)
	v_mfma_f32_16x16x32_f16 v[8:11], v[104:107], v[68:71], v[8:11]
	v_mfma_f32_16x16x32_f16 v[40:43], v[104:107], v[84:87], v[40:43]
	s_waitcnt vmcnt(17)
	v_mfma_f32_16x16x32_f16 v[12:15], v[108:111], v[68:71], v[12:15]
	v_mfma_f32_16x16x32_f16 v[44:47], v[108:111], v[84:87], v[44:47]
	s_waitcnt vmcnt(16)
	v_mfma_f32_16x16x32_f16 v[16:19], v[112:115], v[68:71], v[16:19]
	v_mfma_f32_16x16x32_f16 v[48:51], v[112:115], v[84:87], v[48:51]
	s_waitcnt vmcnt(15)
	v_mfma_f32_16x16x32_f16 v[20:23], v[116:119], v[68:71], v[20:23]
	v_mfma_f32_16x16x32_f16 v[52:55], v[116:119], v[84:87], v[52:55]
	s_waitcnt vmcnt(14)
	v_mfma_f32_16x16x32_f16 v[24:27], v[120:123], v[68:71], v[24:27]
	v_mfma_f32_16x16x32_f16 v[56:59], v[120:123], v[84:87], v[56:59]
	s_waitcnt vmcnt(13)
	v_mfma_f32_16x16x32_f16 v[28:31], v[124:127], v[68:71], v[28:31]
	v_mfma_f32_16x16x32_f16 v[60:63], v[124:127], v[84:87], v[60:63]
	s_waitcnt vmcnt(12)
	v_mfma_f32_16x16x32_f16 v[32:35], v[128:131], v[68:71], v[32:35]
	v_mfma_f32_16x16x32_f16 v[64:67], v[128:131], v[84:87], v[64:67]
	global_load_dwordx4 v[100:103], v166, s[6:7] offset:0
	global_load_dwordx4 v[104:107], v166, s[6:7] offset:1024
	global_load_dwordx4 v[108:111], v166, s[6:7] offset:2048
	global_load_dwordx4 v[112:115], v166, s[6:7] offset:3072
	global_load_dwordx4 v[116:119], v167, s[6:7] offset:0
	global_load_dwordx4 v[120:123], v167, s[6:7] offset:1024
	global_load_dwordx4 v[124:127], v167, s[6:7] offset:2048
	global_load_dwordx4 v[128:131], v167, s[6:7] offset:3072
	s_add_u32 s6, s6, 0x2000
	s_addc_u32 s7, s7, 0
	global_load_dwordx4 v[68:71], v164, s[10:11]
	global_load_dwordx4 v[84:87], v165, s[10:11]
	s_add_u32 s10, s10, 0x9c400
	s_addc_u32 s11, s11, 0
	s_waitcnt vmcnt(19)
	v_mfma_f32_16x16x32_f16 v[4:7], v[132:135], v[72:75], v[4:7]
	v_mfma_f32_16x16x32_f16 v[36:39], v[132:135], v[88:91], v[36:39]
	s_waitcnt vmcnt(18)
	v_mfma_f32_16x16x32_f16 v[8:11], v[136:139], v[72:75], v[8:11]
	v_mfma_f32_16x16x32_f16 v[40:43], v[136:139], v[88:91], v[40:43]
	s_waitcnt vmcnt(17)
	v_mfma_f32_16x16x32_f16 v[12:15], v[140:143], v[72:75], v[12:15]
	v_mfma_f32_16x16x32_f16 v[44:47], v[140:143], v[88:91], v[44:47]
	s_waitcnt vmcnt(16)
	v_mfma_f32_16x16x32_f16 v[16:19], v[144:147], v[72:75], v[16:19]
	v_mfma_f32_16x16x32_f16 v[48:51], v[144:147], v[88:91], v[48:51]
	s_waitcnt vmcnt(15)
	v_mfma_f32_16x16x32_f16 v[20:23], v[148:151], v[72:75], v[20:23]
	v_mfma_f32_16x16x32_f16 v[52:55], v[148:151], v[88:91], v[52:55]
	s_waitcnt vmcnt(14)
	v_mfma_f32_16x16x32_f16 v[24:27], v[152:155], v[72:75], v[24:27]
	v_mfma_f32_16x16x32_f16 v[56:59], v[152:155], v[88:91], v[56:59]
	s_waitcnt vmcnt(13)
	v_mfma_f32_16x16x32_f16 v[28:31], v[156:159], v[72:75], v[28:31]
	v_mfma_f32_16x16x32_f16 v[60:63], v[156:159], v[88:91], v[60:63]
	s_waitcnt vmcnt(12)
	v_mfma_f32_16x16x32_f16 v[32:35], v[160:163], v[72:75], v[32:35]
	v_mfma_f32_16x16x32_f16 v[64:67], v[160:163], v[88:91], v[64:67]
	global_load_dwordx4 v[132:135], v166, s[6:7] offset:0
	global_load_dwordx4 v[136:139], v166, s[6:7] offset:1024
	global_load_dwordx4 v[140:143], v166, s[6:7] offset:2048
	global_load_dwordx4 v[144:147], v166, s[6:7] offset:3072
	global_load_dwordx4 v[148:151], v167, s[6:7] offset:0
	global_load_dwordx4 v[152:155], v167, s[6:7] offset:1024
	global_load_dwordx4 v[156:159], v167, s[6:7] offset:2048
	global_load_dwordx4 v[160:163], v167, s[6:7] offset:3072
	s_add_u32 s6, s6, 0x2000
	s_addc_u32 s7, s7, 0
	global_load_dwordx4 v[72:75], v164, s[10:11]
	global_load_dwordx4 v[88:91], v165, s[10:11]
	s_add_u32 s10, s10, 0x9c400
	s_addc_u32 s11, s11, 0
	s_waitcnt vmcnt(19)
	v_mfma_f32_16x16x32_f16 v[4:7], v[100:103], v[76:79], v[4:7]
	v_mfma_f32_16x16x32_f16 v[36:39], v[100:103], v[92:95], v[36:39]
	s_waitcnt vmcnt(18)
	v_mfma_f32_16x16x32_f16 v[8:11], v[104:107], v[76:79], v[8:11]
	v_mfma_f32_16x16x32_f16 v[40:43], v[104:107], v[92:95], v[40:43]
	s_waitcnt vmcnt(17)
	v_mfma_f32_16x16x32_f16 v[12:15], v[108:111], v[76:79], v[12:15]
	v_mfma_f32_16x16x32_f16 v[44:47], v[108:111], v[92:95], v[44:47]
	s_waitcnt vmcnt(16)
	v_mfma_f32_16x16x32_f16 v[16:19], v[112:115], v[76:79], v[16:19]
	v_mfma_f32_16x16x32_f16 v[48:51], v[112:115], v[92:95], v[48:51]
	s_waitcnt vmcnt(15)
	v_mfma_f32_16x16x32_f16 v[20:23], v[116:119], v[76:79], v[20:23]
	v_mfma_f32_16x16x32_f16 v[52:55], v[116:119], v[92:95], v[52:55]
	s_waitcnt vmcnt(14)
	v_mfma_f32_16x16x32_f16 v[24:27], v[120:123], v[76:79], v[24:27]
	v_mfma_f32_16x16x32_f16 v[56:59], v[120:123], v[92:95], v[56:59]
	s_waitcnt vmcnt(13)
	v_mfma_f32_16x16x32_f16 v[28:31], v[124:127], v[76:79], v[28:31]
	v_mfma_f32_16x16x32_f16 v[60:63], v[124:127], v[92:95], v[60:63]
	s_waitcnt vmcnt(12)
	v_mfma_f32_16x16x32_f16 v[32:35], v[128:131], v[76:79], v[32:35]
	v_mfma_f32_16x16x32_f16 v[64:67], v[128:131], v[92:95], v[64:67]
	global_load_dwordx4 v[100:103], v166, s[6:7] offset:0
	global_load_dwordx4 v[104:107], v166, s[6:7] offset:1024
	global_load_dwordx4 v[108:111], v166, s[6:7] offset:2048
	global_load_dwordx4 v[112:115], v166, s[6:7] offset:3072
	global_load_dwordx4 v[116:119], v167, s[6:7] offset:0
	global_load_dwordx4 v[120:123], v167, s[6:7] offset:1024
	global_load_dwordx4 v[124:127], v167, s[6:7] offset:2048
	global_load_dwordx4 v[128:131], v167, s[6:7] offset:3072
	s_add_u32 s6, s6, 0x2000
	s_addc_u32 s7, s7, 0
	global_load_dwordx4 v[76:79], v164, s[10:11]
	global_load_dwordx4 v[92:95], v165, s[10:11]
	s_add_u32 s10, s10, 0x9c400
	s_addc_u32 s11, s11, 0
	s_waitcnt vmcnt(19)
	v_mfma_f32_16x16x32_f16 v[4:7], v[132:135], v[80:83], v[4:7]
	v_mfma_f32_16x16x32_f16 v[36:39], v[132:135], v[96:99], v[36:39]
	s_waitcnt vmcnt(18)
	v_mfma_f32_16x16x32_f16 v[8:11], v[136:139], v[80:83], v[8:11]
	v_mfma_f32_16x16x32_f16 v[40:43], v[136:139], v[96:99], v[40:43]
	s_waitcnt vmcnt(17)
	v_mfma_f32_16x16x32_f16 v[12:15], v[140:143], v[80:83], v[12:15]
	v_mfma_f32_16x16x32_f16 v[44:47], v[140:143], v[96:99], v[44:47]
	s_waitcnt vmcnt(16)
	v_mfma_f32_16x16x32_f16 v[16:19], v[144:147], v[80:83], v[16:19]
	v_mfma_f32_16x16x32_f16 v[48:51], v[144:147], v[96:99], v[48:51]
	s_waitcnt vmcnt(15)
	v_mfma_f32_16x16x32_f16 v[20:23], v[148:151], v[80:83], v[20:23]
	v_mfma_f32_16x16x32_f16 v[52:55], v[148:151], v[96:99], v[52:55]
	s_waitcnt vmcnt(14)
	v_mfma_f32_16x16x32_f16 v[24:27], v[152:155], v[80:83], v[24:27]
	v_mfma_f32_16x16x32_f16 v[56:59], v[152:155], v[96:99], v[56:59]
	s_waitcnt vmcnt(13)
	v_mfma_f32_16x16x32_f16 v[28:31], v[156:159], v[80:83], v[28:31]
	v_mfma_f32_16x16x32_f16 v[60:63], v[156:159], v[96:99], v[60:63]
	s_waitcnt vmcnt(12)
	v_mfma_f32_16x16x32_f16 v[32:35], v[160:163], v[80:83], v[32:35]
	v_mfma_f32_16x16x32_f16 v[64:67], v[160:163], v[96:99], v[64:67]
	global_load_dwordx4 v[132:135], v166, s[6:7] offset:0
	global_load_dwordx4 v[136:139], v166, s[6:7] offset:1024
	global_load_dwordx4 v[140:143], v166, s[6:7] offset:2048
	global_load_dwordx4 v[144:147], v166, s[6:7] offset:3072
	global_load_dwordx4 v[148:151], v167, s[6:7] offset:0
	global_load_dwordx4 v[152:155], v167, s[6:7] offset:1024
	global_load_dwordx4 v[156:159], v167, s[6:7] offset:2048
	global_load_dwordx4 v[160:163], v167, s[6:7] offset:3072
	s_add_u32 s6, s6, 0x2000
	s_addc_u32 s7, s7, 0
	global_load_dwordx4 v[80:83], v164, s[10:11]
	global_load_dwordx4 v[96:99], v165, s[10:11]
	s_add_u32 s10, s10, 0x9c400
	s_addc_u32 s11, s11, 0
	s_waitcnt vmcnt(19)
	v_mfma_f32_16x16x32_f16 v[4:7], v[100:103], v[68:71], v[4:7]
	v_mfma_f32_16x16x32_f16 v[36:39], v[100:103], v[84:87], v[36:39]
	s_waitcnt vmcnt(18)
	v_mfma_f32_16x16x32_f16 v[8:11], v[104:107], v[68:71], v[8:11]
	v_mfma_f32_16x16x32_f16 v[40:43], v[104:107], v[84:87], v[40:43]
	s_waitcnt vmcnt(17)
	v_mfma_f32_16x16x32_f16 v[12:15], v[108:111], v[68:71], v[12:15]
	v_mfma_f32_16x16x32_f16 v[44:47], v[108:111], v[84:87], v[44:47]
	s_waitcnt vmcnt(16)
	v_mfma_f32_16x16x32_f16 v[16:19], v[112:115], v[68:71], v[16:19]
	v_mfma_f32_16x16x32_f16 v[48:51], v[112:115], v[84:87], v[48:51]
	s_waitcnt vmcnt(15)
	v_mfma_f32_16x16x32_f16 v[20:23], v[116:119], v[68:71], v[20:23]
	v_mfma_f32_16x16x32_f16 v[52:55], v[116:119], v[84:87], v[52:55]
	s_waitcnt vmcnt(14)
	v_mfma_f32_16x16x32_f16 v[24:27], v[120:123], v[68:71], v[24:27]
	v_mfma_f32_16x16x32_f16 v[56:59], v[120:123], v[84:87], v[56:59]
	s_waitcnt vmcnt(13)
	v_mfma_f32_16x16x32_f16 v[28:31], v[124:127], v[68:71], v[28:31]
	v_mfma_f32_16x16x32_f16 v[60:63], v[124:127], v[84:87], v[60:63]
	s_waitcnt vmcnt(12)
	v_mfma_f32_16x16x32_f16 v[32:35], v[128:131], v[68:71], v[32:35]
	v_mfma_f32_16x16x32_f16 v[64:67], v[128:131], v[84:87], v[64:67]
	global_load_dwordx4 v[100:103], v166, s[6:7] offset:0
	global_load_dwordx4 v[104:107], v166, s[6:7] offset:1024
	global_load_dwordx4 v[108:111], v166, s[6:7] offset:2048
	global_load_dwordx4 v[112:115], v166, s[6:7] offset:3072
	global_load_dwordx4 v[116:119], v167, s[6:7] offset:0
	global_load_dwordx4 v[120:123], v167, s[6:7] offset:1024
	global_load_dwordx4 v[124:127], v167, s[6:7] offset:2048
	global_load_dwordx4 v[128:131], v167, s[6:7] offset:3072
	s_add_u32 s6, s6, 0x2000
	s_addc_u32 s7, s7, 0
	global_load_dwordx4 v[68:71], v164, s[10:11]
	global_load_dwordx4 v[84:87], v165, s[10:11]
	s_add_u32 s10, s10, 0x9c400
	s_addc_u32 s11, s11, 0
	s_waitcnt vmcnt(19)
	v_mfma_f32_16x16x32_f16 v[4:7], v[132:135], v[72:75], v[4:7]
	v_mfma_f32_16x16x32_f16 v[36:39], v[132:135], v[88:91], v[36:39]
	s_waitcnt vmcnt(18)
	v_mfma_f32_16x16x32_f16 v[8:11], v[136:139], v[72:75], v[8:11]
	v_mfma_f32_16x16x32_f16 v[40:43], v[136:139], v[88:91], v[40:43]
	s_waitcnt vmcnt(17)
	v_mfma_f32_16x16x32_f16 v[12:15], v[140:143], v[72:75], v[12:15]
	v_mfma_f32_16x16x32_f16 v[44:47], v[140:143], v[88:91], v[44:47]
	s_waitcnt vmcnt(16)
	v_mfma_f32_16x16x32_f16 v[16:19], v[144:147], v[72:75], v[16:19]
	v_mfma_f32_16x16x32_f16 v[48:51], v[144:147], v[88:91], v[48:51]
	s_waitcnt vmcnt(15)
	v_mfma_f32_16x16x32_f16 v[20:23], v[148:151], v[72:75], v[20:23]
	v_mfma_f32_16x16x32_f16 v[52:55], v[148:151], v[88:91], v[52:55]
	s_waitcnt vmcnt(14)
	v_mfma_f32_16x16x32_f16 v[24:27], v[152:155], v[72:75], v[24:27]
	v_mfma_f32_16x16x32_f16 v[56:59], v[152:155], v[88:91], v[56:59]
	s_waitcnt vmcnt(13)
	v_mfma_f32_16x16x32_f16 v[28:31], v[156:159], v[72:75], v[28:31]
	v_mfma_f32_16x16x32_f16 v[60:63], v[156:159], v[88:91], v[60:63]
	s_waitcnt vmcnt(12)
	v_mfma_f32_16x16x32_f16 v[32:35], v[160:163], v[72:75], v[32:35]
	v_mfma_f32_16x16x32_f16 v[64:67], v[160:163], v[88:91], v[64:67]
	global_load_dwordx4 v[132:135], v166, s[6:7] offset:0
	global_load_dwordx4 v[136:139], v166, s[6:7] offset:1024
	global_load_dwordx4 v[140:143], v166, s[6:7] offset:2048
	global_load_dwordx4 v[144:147], v166, s[6:7] offset:3072
	global_load_dwordx4 v[148:151], v167, s[6:7] offset:0
	global_load_dwordx4 v[152:155], v167, s[6:7] offset:1024
	global_load_dwordx4 v[156:159], v167, s[6:7] offset:2048
	global_load_dwordx4 v[160:163], v167, s[6:7] offset:3072
	s_add_u32 s6, s6, 0x2000
	s_addc_u32 s7, s7, 0
	global_load_dwordx4 v[72:75], v164, s[10:11]
	global_load_dwordx4 v[88:91], v165, s[10:11]
	s_add_u32 s10, s10, 0x9c400
	s_addc_u32 s11, s11, 0
	s_waitcnt vmcnt(19)
	v_mfma_f32_16x16x32_f16 v[4:7], v[100:103], v[76:79], v[4:7]
	v_mfma_f32_16x16x32_f16 v[36:39], v[100:103], v[92:95], v[36:39]
	s_waitcnt vmcnt(18)
	v_mfma_f32_16x16x32_f16 v[8:11], v[104:107], v[76:79], v[8:11]
	v_mfma_f32_16x16x32_f16 v[40:43], v[104:107], v[92:95], v[40:43]
	s_waitcnt vmcnt(17)
	v_mfma_f32_16x16x32_f16 v[12:15], v[108:111], v[76:79], v[12:15]
	v_mfma_f32_16x16x32_f16 v[44:47], v[108:111], v[92:95], v[44:47]
	s_waitcnt vmcnt(16)
	v_mfma_f32_16x16x32_f16 v[16:19], v[112:115], v[76:79], v[16:19]
	v_mfma_f32_16x16x32_f16 v[48:51], v[112:115], v[92:95], v[48:51]
	s_waitcnt vmcnt(15)
	v_mfma_f32_16x16x32_f16 v[20:23], v[116:119], v[76:79], v[20:23]
	v_mfma_f32_16x16x32_f16 v[52:55], v[116:119], v[92:95], v[52:55]
	s_waitcnt vmcnt(14)
	v_mfma_f32_16x16x32_f16 v[24:27], v[120:123], v[76:79], v[24:27]
	v_mfma_f32_16x16x32_f16 v[56:59], v[120:123], v[92:95], v[56:59]
	s_waitcnt vmcnt(13)
	v_mfma_f32_16x16x32_f16 v[28:31], v[124:127], v[76:79], v[28:31]
	v_mfma_f32_16x16x32_f16 v[60:63], v[124:127], v[92:95], v[60:63]
	s_waitcnt vmcnt(12)
	v_mfma_f32_16x16x32_f16 v[32:35], v[128:131], v[76:79], v[32:35]
	v_mfma_f32_16x16x32_f16 v[64:67], v[128:131], v[92:95], v[64:67]
	global_load_dwordx4 v[100:103], v166, s[6:7] offset:0
	global_load_dwordx4 v[104:107], v166, s[6:7] offset:1024
	global_load_dwordx4 v[108:111], v166, s[6:7] offset:2048
	global_load_dwordx4 v[112:115], v166, s[6:7] offset:3072
	global_load_dwordx4 v[116:119], v167, s[6:7] offset:0
	global_load_dwordx4 v[120:123], v167, s[6:7] offset:1024
	global_load_dwordx4 v[124:127], v167, s[6:7] offset:2048
	global_load_dwordx4 v[128:131], v167, s[6:7] offset:3072
	s_add_u32 s6, s6, 0x2000
	s_addc_u32 s7, s7, 0
	global_load_dwordx4 v[76:79], v164, s[10:11]
	global_load_dwordx4 v[92:95], v165, s[10:11]
	s_add_u32 s10, s10, 0x9c400
	s_addc_u32 s11, s11, 0
	s_waitcnt vmcnt(19)
	v_mfma_f32_16x16x32_f16 v[4:7], v[132:135], v[80:83], v[4:7]
	v_mfma_f32_16x16x32_f16 v[36:39], v[132:135], v[96:99], v[36:39]
	s_waitcnt vmcnt(18)
	v_mfma_f32_16x16x32_f16 v[8:11], v[136:139], v[80:83], v[8:11]
	v_mfma_f32_16x16x32_f16 v[40:43], v[136:139], v[96:99], v[40:43]
	s_waitcnt vmcnt(17)
	v_mfma_f32_16x16x32_f16 v[12:15], v[140:143], v[80:83], v[12:15]
	v_mfma_f32_16x16x32_f16 v[44:47], v[140:143], v[96:99], v[44:47]
	s_waitcnt vmcnt(16)
	v_mfma_f32_16x16x32_f16 v[16:19], v[144:147], v[80:83], v[16:19]
	v_mfma_f32_16x16x32_f16 v[48:51], v[144:147], v[96:99], v[48:51]
	s_waitcnt vmcnt(15)
	v_mfma_f32_16x16x32_f16 v[20:23], v[148:151], v[80:83], v[20:23]
	v_mfma_f32_16x16x32_f16 v[52:55], v[148:151], v[96:99], v[52:55]
	s_waitcnt vmcnt(14)
	v_mfma_f32_16x16x32_f16 v[24:27], v[152:155], v[80:83], v[24:27]
	v_mfma_f32_16x16x32_f16 v[56:59], v[152:155], v[96:99], v[56:59]
	s_waitcnt vmcnt(13)
	v_mfma_f32_16x16x32_f16 v[28:31], v[156:159], v[80:83], v[28:31]
	v_mfma_f32_16x16x32_f16 v[60:63], v[156:159], v[96:99], v[60:63]
	s_waitcnt vmcnt(12)
	v_mfma_f32_16x16x32_f16 v[32:35], v[160:163], v[80:83], v[32:35]
	v_mfma_f32_16x16x32_f16 v[64:67], v[160:163], v[96:99], v[64:67]
	global_load_dwordx4 v[132:135], v166, s[6:7] offset:0
	global_load_dwordx4 v[136:139], v166, s[6:7] offset:1024
	global_load_dwordx4 v[140:143], v166, s[6:7] offset:2048
	global_load_dwordx4 v[144:147], v166, s[6:7] offset:3072
	global_load_dwordx4 v[148:151], v167, s[6:7] offset:0
	global_load_dwordx4 v[152:155], v167, s[6:7] offset:1024
	global_load_dwordx4 v[156:159], v167, s[6:7] offset:2048
	global_load_dwordx4 v[160:163], v167, s[6:7] offset:3072
	s_add_u32 s6, s6, 0x2000
	s_addc_u32 s7, s7, 0
	global_load_dwordx4 v[80:83], v164, s[10:11]
	global_load_dwordx4 v[96:99], v165, s[10:11]
	s_add_u32 s10, s10, 0x9c400
	s_addc_u32 s11, s11, 0
	s_waitcnt vmcnt(19)
	v_mfma_f32_16x16x32_f16 v[4:7], v[100:103], v[68:71], v[4:7]
	v_mfma_f32_16x16x32_f16 v[36:39], v[100:103], v[84:87], v[36:39]
	s_waitcnt vmcnt(18)
	v_mfma_f32_16x16x32_f16 v[8:11], v[104:107], v[68:71], v[8:11]
	v_mfma_f32_16x16x32_f16 v[40:43], v[104:107], v[84:87], v[40:43]
	s_waitcnt vmcnt(17)
	v_mfma_f32_16x16x32_f16 v[12:15], v[108:111], v[68:71], v[12:15]
	v_mfma_f32_16x16x32_f16 v[44:47], v[108:111], v[84:87], v[44:47]
	s_waitcnt vmcnt(16)
	v_mfma_f32_16x16x32_f16 v[16:19], v[112:115], v[68:71], v[16:19]
	v_mfma_f32_16x16x32_f16 v[48:51], v[112:115], v[84:87], v[48:51]
	s_waitcnt vmcnt(15)
	v_mfma_f32_16x16x32_f16 v[20:23], v[116:119], v[68:71], v[20:23]
	v_mfma_f32_16x16x32_f16 v[52:55], v[116:119], v[84:87], v[52:55]
	s_waitcnt vmcnt(14)
	v_mfma_f32_16x16x32_f16 v[24:27], v[120:123], v[68:71], v[24:27]
	v_mfma_f32_16x16x32_f16 v[56:59], v[120:123], v[84:87], v[56:59]
	s_waitcnt vmcnt(13)
	v_mfma_f32_16x16x32_f16 v[28:31], v[124:127], v[68:71], v[28:31]
	v_mfma_f32_16x16x32_f16 v[60:63], v[124:127], v[84:87], v[60:63]
	s_waitcnt vmcnt(12)
	v_mfma_f32_16x16x32_f16 v[32:35], v[128:131], v[68:71], v[32:35]
	v_mfma_f32_16x16x32_f16 v[64:67], v[128:131], v[84:87], v[64:67]
	global_load_dwordx4 v[100:103], v166, s[6:7] offset:0
	global_load_dwordx4 v[104:107], v166, s[6:7] offset:1024
	global_load_dwordx4 v[108:111], v166, s[6:7] offset:2048
	global_load_dwordx4 v[112:115], v166, s[6:7] offset:3072
	global_load_dwordx4 v[116:119], v167, s[6:7] offset:0
	global_load_dwordx4 v[120:123], v167, s[6:7] offset:1024
	global_load_dwordx4 v[124:127], v167, s[6:7] offset:2048
	global_load_dwordx4 v[128:131], v167, s[6:7] offset:3072
	s_add_u32 s6, s6, 0x2000
	s_addc_u32 s7, s7, 0
	s_waitcnt vmcnt(17)
	v_mfma_f32_16x16x32_f16 v[4:7], v[132:135], v[72:75], v[4:7]
	v_mfma_f32_16x16x32_f16 v[36:39], v[132:135], v[88:91], v[36:39]
	s_waitcnt vmcnt(16)
	v_mfma_f32_16x16x32_f16 v[8:11], v[136:139], v[72:75], v[8:11]
	v_mfma_f32_16x16x32_f16 v[40:43], v[136:139], v[88:91], v[40:43]
	s_waitcnt vmcnt(15)
	v_mfma_f32_16x16x32_f16 v[12:15], v[140:143], v[72:75], v[12:15]
	v_mfma_f32_16x16x32_f16 v[44:47], v[140:143], v[88:91], v[44:47]
	s_waitcnt vmcnt(14)
	v_mfma_f32_16x16x32_f16 v[16:19], v[144:147], v[72:75], v[16:19]
	v_mfma_f32_16x16x32_f16 v[48:51], v[144:147], v[88:91], v[48:51]
	s_waitcnt vmcnt(13)
	v_mfma_f32_16x16x32_f16 v[20:23], v[148:151], v[72:75], v[20:23]
	v_mfma_f32_16x16x32_f16 v[52:55], v[148:151], v[88:91], v[52:55]
	s_waitcnt vmcnt(12)
	v_mfma_f32_16x16x32_f16 v[24:27], v[152:155], v[72:75], v[24:27]
	v_mfma_f32_16x16x32_f16 v[56:59], v[152:155], v[88:91], v[56:59]
	s_waitcnt vmcnt(11)
	v_mfma_f32_16x16x32_f16 v[28:31], v[156:159], v[72:75], v[28:31]
	v_mfma_f32_16x16x32_f16 v[60:63], v[156:159], v[88:91], v[60:63]
	s_waitcnt vmcnt(10)
	v_mfma_f32_16x16x32_f16 v[32:35], v[160:163], v[72:75], v[32:35]
	v_mfma_f32_16x16x32_f16 v[64:67], v[160:163], v[88:91], v[64:67]
	global_load_dwordx4 v[132:135], v166, s[6:7] offset:0
	global_load_dwordx4 v[136:139], v166, s[6:7] offset:1024
	global_load_dwordx4 v[140:143], v166, s[6:7] offset:2048
	global_load_dwordx4 v[144:147], v166, s[6:7] offset:3072
	global_load_dwordx4 v[148:151], v167, s[6:7] offset:0
	global_load_dwordx4 v[152:155], v167, s[6:7] offset:1024
	global_load_dwordx4 v[156:159], v167, s[6:7] offset:2048
	global_load_dwordx4 v[160:163], v167, s[6:7] offset:3072
	s_add_u32 s6, s6, 0x2000
	s_addc_u32 s7, s7, 0
	s_waitcnt vmcnt(15)
	v_mfma_f32_16x16x32_f16 v[4:7], v[100:103], v[76:79], v[4:7]
	v_mfma_f32_16x16x32_f16 v[36:39], v[100:103], v[92:95], v[36:39]
	s_waitcnt vmcnt(14)
	v_mfma_f32_16x16x32_f16 v[8:11], v[104:107], v[76:79], v[8:11]
	v_mfma_f32_16x16x32_f16 v[40:43], v[104:107], v[92:95], v[40:43]
	s_waitcnt vmcnt(13)
	v_mfma_f32_16x16x32_f16 v[12:15], v[108:111], v[76:79], v[12:15]
	v_mfma_f32_16x16x32_f16 v[44:47], v[108:111], v[92:95], v[44:47]
	s_waitcnt vmcnt(12)
	v_mfma_f32_16x16x32_f16 v[16:19], v[112:115], v[76:79], v[16:19]
	v_mfma_f32_16x16x32_f16 v[48:51], v[112:115], v[92:95], v[48:51]
	s_waitcnt vmcnt(11)
	v_mfma_f32_16x16x32_f16 v[20:23], v[116:119], v[76:79], v[20:23]
	v_mfma_f32_16x16x32_f16 v[52:55], v[116:119], v[92:95], v[52:55]
	s_waitcnt vmcnt(10)
	v_mfma_f32_16x16x32_f16 v[24:27], v[120:123], v[76:79], v[24:27]
	v_mfma_f32_16x16x32_f16 v[56:59], v[120:123], v[92:95], v[56:59]
	s_waitcnt vmcnt(9)
	v_mfma_f32_16x16x32_f16 v[28:31], v[124:127], v[76:79], v[28:31]
	v_mfma_f32_16x16x32_f16 v[60:63], v[124:127], v[92:95], v[60:63]
	s_waitcnt vmcnt(8)
	v_mfma_f32_16x16x32_f16 v[32:35], v[128:131], v[76:79], v[32:35]
	v_mfma_f32_16x16x32_f16 v[64:67], v[128:131], v[92:95], v[64:67]
	s_waitcnt vmcnt(7)
	v_mfma_f32_16x16x32_f16 v[4:7], v[132:135], v[80:83], v[4:7]
	v_mfma_f32_16x16x32_f16 v[36:39], v[132:135], v[96:99], v[36:39]
	s_waitcnt vmcnt(6)
	v_mfma_f32_16x16x32_f16 v[8:11], v[136:139], v[80:83], v[8:11]
	v_mfma_f32_16x16x32_f16 v[40:43], v[136:139], v[96:99], v[40:43]
	s_waitcnt vmcnt(5)
	v_mfma_f32_16x16x32_f16 v[12:15], v[140:143], v[80:83], v[12:15]
	v_mfma_f32_16x16x32_f16 v[44:47], v[140:143], v[96:99], v[44:47]
	s_waitcnt vmcnt(4)
	v_mfma_f32_16x16x32_f16 v[16:19], v[144:147], v[80:83], v[16:19]
	v_mfma_f32_16x16x32_f16 v[48:51], v[144:147], v[96:99], v[48:51]
	s_waitcnt vmcnt(3)
	v_mfma_f32_16x16x32_f16 v[20:23], v[148:151], v[80:83], v[20:23]
	v_mfma_f32_16x16x32_f16 v[52:55], v[148:151], v[96:99], v[52:55]
	s_waitcnt vmcnt(2)
	v_mfma_f32_16x16x32_f16 v[24:27], v[152:155], v[80:83], v[24:27]
	v_mfma_f32_16x16x32_f16 v[56:59], v[152:155], v[96:99], v[56:59]
	s_waitcnt vmcnt(1)
	v_mfma_f32_16x16x32_f16 v[28:31], v[156:159], v[80:83], v[28:31]
	v_mfma_f32_16x16x32_f16 v[60:63], v[156:159], v[96:99], v[60:63]
	s_waitcnt vmcnt(0)
	v_mfma_f32_16x16x32_f16 v[32:35], v[160:163], v[80:83], v[32:35]
	v_mfma_f32_16x16x32_f16 v[64:67], v[160:163], v[96:99], v[64:67]
	s_nop 7
	s_nop 1
	global_store_dwordx4 v168, v[4:7], s[8:9] offset:0
	global_store_dwordx4 v168, v[8:11], s[8:9] offset:64
	global_store_dwordx4 v168, v[12:15], s[8:9] offset:128
	global_store_dwordx4 v168, v[16:19], s[8:9] offset:192
	global_store_dwordx4 v168, v[20:23], s[8:9] offset:256
	global_store_dwordx4 v168, v[24:27], s[8:9] offset:320
	global_store_dwordx4 v168, v[28:31], s[8:9] offset:384
	global_store_dwordx4 v168, v[32:35], s[8:9] offset:448
	s_cmp_eq_u32 s23, 0
	s_cbranch_scc1 .LBB6_39
	global_store_dwordx4 v169, v[36:39], s[8:9] offset:0
	global_store_dwordx4 v169, v[40:43], s[8:9] offset:64
	global_store_dwordx4 v169, v[44:47], s[8:9] offset:128
	global_store_dwordx4 v169, v[48:51], s[8:9] offset:192
	global_store_dwordx4 v169, v[52:55], s[8:9] offset:256
	global_store_dwordx4 v169, v[56:59], s[8:9] offset:320
	global_store_dwordx4 v169, v[60:63], s[8:9] offset:384
	global_store_dwordx4 v169, v[64:67], s[8:9] offset:448
	s_branch .LBB6_39
